# baseline (speedup 1.0000x reference)
.Lk2f_l3:
	s_waitcnt vmcnt(0)
	s_cmp_lt_u32 s4, 4
	s_cbranch_scc0 .Lk2f_l4
	v_sub_u32_e32 v24, v9, v8
	v_min_u32_e32 v25, 0xf4, v0
	v_lshlrev_b32_e32 v25, 14, v25
	v_lshl_add_u32 v25, v8, 2, v25
	v_cmp_lt_i32_e64 s[38:39], 0, v24
	v_cmp_lt_i32_e64 s[40:41], 4, v24
	v_cmp_lt_i32_e64 s[42:43], 8, v24
	v_cmp_lt_i32_e64 s[44:45], 12, v24
	s_mov_b64 exec, s[38:39]
	s_cbranch_execz .Lk2f_p0
	global_load_dwordx4 v[26:29], v25, s[10:11]
